# combo7 + static priority raise (s_setprio 1) for waves 0-3 during the mLSTM / attention phase
# baseline (speedup 1.0000x reference)
.LBB0_507:
	s_cmp_lt_i32 s48, 4
	s_cselect_b64 s[6:7], -1, 0
	s_and_b64 s[28:29], s[6:7], s[4:5]
	s_andn2_b64 vcc, exec, s[28:29]
	s_cbranch_vccnz .LBB0_561
	v_readfirstlane_b32 s6, v0
	s_nop 3
	s_bitcmp0_b32 s6, 8
	s_cbranch_scc0 .Lprio3_done
	s_setprio 1
